# v55 + P11 selected-key list load prefetched one query ahead
# baseline (speedup 1.0000x reference)
.LBB0_1449:
	s_or_b64 exec, exec, s[16:17]
	v_ashrrev_i32_e32 v1, 31, v0
	v_lshl_add_u64 v[2:3], v[0:1], 2, s[14:15]
	global_load_dword v2, v[2:3], off
	v_lshl_add_u32 v1, v0, 2, 0
	v_add_u32_e32 v1, 0x24000, v1
	v_cmp_gt_i32_e32 vcc, 16, v0
	s_waitcnt vmcnt(0)
	v_mul_f32_e32 v2, 0x3fb8aa3b, v2
	ds_write_b32 v1, v2
	s_and_saveexec_b64 s[2:3], vcc
	v_mov_b32_e32 v0, 0xff800000
	ds_write_b32 v1, v0 offset:2048
	s_or_b64 exec, exec, s[2:3]
	s_lshl_b32 s2, s93, 14
	s_add_i32 s23, s2, 0
	s_lshl_b32 s2, s88, 3
	s_add_i32 s15, s2, s93
	s_lshl_b32 s22, s96, 3
	s_cmpk_gt_i32 s15, 0x7fff
	s_waitcnt lgkmcnt(0)
	s_barrier
	s_cbranch_scc1 .LBB0_1478
	s_add_u32 s24, s0, 0x12c00000
	s_addc_u32 s25, s1, 0
	s_add_u32 s26, s0, 0x28000000
	s_addc_u32 s27, s1, 0
	s_add_u32 s4, s0, 0x27000000
	s_addc_u32 s5, s1, 0
	s_add_u32 s28, s0, 0x26000000
	s_addc_u32 s29, s1, 0
	s_lshl_b32 s2, s93, 9
	v_and_b32_e32 v159, 64, v6
	s_add_i32 s30, s2, 0
	s_lshl_b32 s2, s93, 8
	v_xor_b32_e32 v0, 16, v6
	v_add_u32_e32 v1, 64, v159
	s_add_i32 s37, s2, 0
	v_cmp_lt_i32_e32 vcc, v0, v1
	s_add_i32 s30, s30, 0x20000
	s_add_i32 s31, s37, 0x21000
	v_cndmask_b32_e32 v0, v6, v0, vcc
	v_lshlrev_b32_e32 v160, 2, v0
	v_xor_b32_e32 v0, 32, v6
	s_add_u32 s33, s0, 0xa000000
	v_cmp_lt_i32_e32 vcc, v0, v1
	s_addc_u32 s34, s1, 0
	s_add_u32 s35, s0, 0x2000000
	v_cndmask_b32_e32 v0, v6, v0, vcc
	s_mov_b32 s7, 0
	v_lshlrev_b32_e32 v161, 2, v0
	s_addc_u32 s36, s1, 0
	s_add_i32 s37, s37, 0x21010
	v_mov_b32_e32 v1, 0
	s_add_i32 s38, 0, 0x24000
	s_mov_b32 s14, 0x3a800000
	s_mov_b32 s39, 0xc3e00000
	s_movk_i32 s40, 0x84
	v_mov_b32_e32 v162, 0x43e00000
	s_lshl_b32 s41, s22, 1
	s_lshl_b32 s42, s22, 5
	s_mov_b32 s43, 0
	s_mov_b32 s16, s15
	s_mov_b32 s44, s15
	s_ashr_i32 s45, s15, 31
	s_lshl_b64 s[44:45], s[44:45], 9
	s_add_u32 s44, s28, s44
	s_addc_u32 s45, s29, s45
	v_mov_b32_e32 v252, v158
	v_mov_b32_e32 v253, 0
	v_lshl_add_u64 v[252:253], v[252:253], 3, s[44:45]
	global_load_dwordx2 v[252:253], v[252:253], off nt
	s_waitcnt vmcnt(0)
	s_branch .LBB0_1454

.LBB0_1454:
	s_ashr_i32 s17, s16, 31
	s_lshr_b32 s2, s17, 19
	s_add_i32 s18, s16, s2
	s_and_b32 s2, s18, 0xffffe000
	s_sub_i32 s20, s16, s2
	s_min_i32 s6, s20, 0xff
	s_lshl_b64 s[2:3], s[16:17], 9
	v_mov_b32_e32 v154, v158
	s_add_u32 s2, s28, s2
	s_addc_u32 s3, s29, s3
	v_ashrrev_i32_e32 v155, 31, v154
	s_waitcnt lgkmcnt(0)
	s_add_i32 s44, s16, s22
	s_ashr_i32 s45, s44, 31
	s_lshl_b64 s[44:45], s[44:45], 9
	s_add_u32 s44, s28, s44
	s_addc_u32 s45, s29, s45
	s_waitcnt vmcnt(2)
	v_mov_b32_e32 v2, v252
	v_mov_b32_e32 v3, v253
	v_lshl_add_u64 v[252:253], v[154:155], 3, s[44:45]
	global_load_dwordx2 v[252:253], v[252:253], off nt
	v_lshlrev_b32_e32 v0, 2, v154
	v_lshl_add_u32 v4, v154, 3, s30
	v_cmp_ge_i32_e32 vcc, s6, v0
	v_sub_u32_sdwa v5, s20, v2 dst_sel:DWORD dst_unused:UNUSED_PAD src0_sel:DWORD src1_sel:WORD_0
	v_cmp_lt_i32_e64 s[2:3], -1, v5
	ds_write_b64 v4, v[2:3]
	s_and_b64 s[44:45], vcc, s[2:3]
	v_mov_b32_e32 v4, 32
	s_and_saveexec_b64 s[2:3], s[44:45]
	v_add_u32_e32 v4, 0, v5
	v_add_u32_e32 v4, 0x22000, v4
	ds_read_u8 v4, v4
	s_or_b64 exec, exec, s[2:3]
	v_sub_u32_sdwa v2, s20, v2 dst_sel:DWORD dst_unused:UNUSED_PAD src0_sel:DWORD src1_sel:WORD_1
	v_cmp_gt_i32_e32 vcc, s6, v0
	v_cmp_lt_i32_e64 s[2:3], -1, v2
	s_and_b64 s[44:45], vcc, s[2:3]
	v_mov_b32_e32 v6, 0x2000
	s_and_saveexec_b64 s[2:3], s[44:45]
	s_cbranch_execz .LBB0_1458
	v_add_u32_e32 v2, 0, v2
	v_add_u32_e32 v2, 0x22000, v2
	ds_read_u8 v2, v2
	s_waitcnt lgkmcnt(0)
	v_lshlrev_b32_e32 v6, 8, v2
